# attention main loop head placed on a 64-byte instruction-cache line boundary (six cold s_nop before the loop)
# baseline (speedup 1.0000x reference)
.LBB0_724:
	v_lshlrev_b32_e32 v32, 1, v118
	v_and_b32_e32 v218, 32, v32
	v_lshrrev_b32_e32 v32, 2, v118
	v_and_or_b32 v32, v32, 3, v236
	v_lshlrev_b32_e32 v217, 6, v32
	v_add_u32_e32 v32, 0, v218
	v_add3_u32 v239, v32, v216, v217
	v_max3_f32 v32, v16, v17, v0
	v_max3_f32 v33, v18, v19, v1
	s_and_b32 s19, s41, 0x3fffffc0
	v_max3_f32 v32, v32, v2, v3
	v_max3_f32 v33, v33, v22, v23
	s_add_i32 s20, s45, 0x100
	v_max3_f32 v32, v32, v20, v21
	v_max3_f32 v33, v33, v6, v7
	s_lshl_b32 s19, s19, 2
	v_max3_f32 v32, v32, v4, v5
	v_max3_f32 v33, v33, v26, v27
	s_lshr_b32 s39, s20, 6
	v_max3_f32 v32, v32, v24, v25
	v_max3_f32 v33, v33, v10, v11
	s_mov_b64 s[20:21], 0x60000
	v_max3_f32 v32, v32, v8, v9
	v_max3_f32 v33, v33, v30, v31
	s_add_i32 s19, s19, 0
	v_max3_f32 v32, v32, v28, v29
	v_max3_f32 v33, v33, v14, v15
	s_cmp_lg_u32 0, -1
	v_max3_f32 v32, v32, v12, v13
	s_mov_b32 s96, 1
	v_max_f32_e32 v32, v32, v33
	s_mov_b32 s22, 0
	v_mov_b32_e32 v33, v32
	s_nop 1
	v_permlane32_swap_b32_e32 v32, v33
	v_max_f32_e32 v32, v32, v33
	v_lshl_add_u32 v235, v214, 2, s19
	v_sub_f32_e32 v64, v0, v32
	v_sub_f32_e32 v0, v17, v32
	v_sub_f32_e32 v16, v16, v32
	v_sub_f32_e32 v65, v1, v32
	v_sub_f32_e32 v1, v18, v32
	v_sub_f32_e32 v66, v2, v32
	v_sub_f32_e32 v2, v19, v32
	s_nop 0
	v_exp_f32_e32 v81, v0
	v_lshl_add_u32 v0, v236, 2, 0
	v_sub_f32_e32 v67, v3, v32
	v_sub_f32_e32 v3, v20, v32
	v_sub_f32_e32 v68, v4, v32
	v_sub_f32_e32 v4, v21, v32
	v_sub_f32_e32 v69, v5, v32
	v_sub_f32_e32 v5, v22, v32
	v_sub_f32_e32 v70, v6, v32
	v_sub_f32_e32 v6, v23, v32
	v_sub_f32_e32 v71, v7, v32
	v_sub_f32_e32 v7, v24, v32
	v_sub_f32_e32 v72, v8, v32
	v_sub_f32_e32 v8, v25, v32
	v_sub_f32_e32 v73, v9, v32
	v_sub_f32_e32 v9, v26, v32
	v_sub_f32_e32 v74, v10, v32
	v_sub_f32_e32 v10, v27, v32
	v_sub_f32_e32 v75, v11, v32
	v_sub_f32_e32 v11, v28, v32
	v_sub_f32_e32 v76, v12, v32
	v_sub_f32_e32 v12, v29, v32
	v_sub_f32_e32 v77, v13, v32
	v_sub_f32_e32 v13, v30, v32
	v_sub_f32_e32 v78, v14, v32
	v_sub_f32_e32 v14, v31, v32
	v_add_u32_e32 v28, 0x15100, v0
	v_sub_f32_e32 v79, v15, v32
	v_exp_f32_e32 v80, v16
	v_exp_f32_e32 v82, v1
	v_exp_f32_e32 v83, v2
	v_exp_f32_e32 v84, v3
	v_exp_f32_e32 v85, v4
	v_exp_f32_e32 v86, v5
	v_exp_f32_e32 v87, v6
	v_exp_f32_e32 v88, v7
	v_exp_f32_e32 v89, v8
	v_exp_f32_e32 v90, v9
	v_exp_f32_e32 v91, v10
	v_exp_f32_e32 v92, v11
	v_exp_f32_e32 v93, v12
	v_exp_f32_e32 v94, v13
	v_exp_f32_e32 v95, v14
	ds_read_b128 v[0:3], v28
	ds_read_b128 v[4:7], v28 offset:32
	ds_read_b128 v[8:11], v28 offset:128
	ds_read_b128 v[12:15], v28 offset:160
	ds_read_b128 v[16:19], v28 offset:64
	ds_read_b128 v[20:23], v28 offset:96
	ds_read_b128 v[24:27], v28 offset:192
	ds_read_b128 v[28:31], v28 offset:224
	s_waitcnt vmcnt(0) lgkmcnt(0)
	s_barrier
	v_add_f32_e32 v202, v97, v32
	v_exp_f32_e32 v64, v64
	s_waitcnt lgkmcnt(7)
	v_pk_add_f32 v[48:49], v[202:203], v[0:1] op_sel_hi:[0,1] neg_lo:[1,0] neg_hi:[1,0]
	v_lshl_add_u64 v[0:1], v[114:115], 0, s[20:21]
	s_mov_b32 s20, m0
	s_mov_b32 m0, s30
	s_nop 0
	global_load_lds_dwordx4 v[0:1], off
	s_mov_b32 m0, s20
	s_mov_b64 s[20:21], 0x20000
	v_lshl_add_u64 v[0:1], v[116:117], 0, s[20:21]
	s_cselect_b32 s20, 0, 0
	s_add_i32 s18, s20, s18
	s_add_i32 s18, s18, 0x8000
	s_mov_b32 s20, m0
	s_mov_b32 m0, s18
	s_nop 0
	global_load_lds_dwordx4 v[0:1], off
	s_mov_b32 m0, s20
	ds_read_b128 v[158:161], v238 offset:8192
	ds_read_b128 v[146:149], v238 offset:8704
	ds_read_b128 v[154:157], v238 offset:10240
	ds_read_b128 v[142:145], v238 offset:10752
	ds_read_b128 v[150:153], v238 offset:12288
	ds_read_b128 v[138:141], v238 offset:12800
	ds_read_b128 v[134:137], v238 offset:14336
	ds_read_b128 v[130:133], v238 offset:14848
	v_exp_f32_e32 v65, v65
	v_exp_f32_e32 v66, v66
	v_exp_f32_e32 v67, v67
	v_exp_f32_e32 v68, v68
	v_exp_f32_e32 v69, v69
	v_exp_f32_e32 v70, v70
	v_exp_f32_e32 v71, v71
	v_exp_f32_e32 v72, v72
	v_exp_f32_e32 v73, v73
	v_exp_f32_e32 v74, v74
	v_exp_f32_e32 v75, v75
	v_exp_f32_e32 v76, v76
	v_exp_f32_e32 v77, v77
	v_exp_f32_e32 v78, v78
	v_exp_f32_e32 v79, v79
	s_waitcnt vmcnt(2) lgkmcnt(0)
	s_barrier
	v_and_b32_e32 v0, 3, v118
	s_waitcnt lgkmcnt(13)
	v_pk_add_f32 v[32:33], v[202:203], v[8:9] op_sel_hi:[0,1] neg_lo:[1,0] neg_hi:[1,0]
	v_pk_add_f32 v[50:51], v[202:203], v[2:3] op_sel_hi:[0,1] neg_lo:[1,0] neg_hi:[1,0]
	v_pk_add_f32 v[34:35], v[202:203], v[10:11] op_sel_hi:[0,1] neg_lo:[1,0] neg_hi:[1,0]
	v_pk_add_f32 v[52:53], v[202:203], v[4:5] op_sel_hi:[0,1] neg_lo:[1,0] neg_hi:[1,0]
	s_waitcnt lgkmcnt(12)
	v_pk_add_f32 v[36:37], v[202:203], v[12:13] op_sel_hi:[0,1] neg_lo:[1,0] neg_hi:[1,0]
	v_pk_add_f32 v[54:55], v[202:203], v[6:7] op_sel_hi:[0,1] neg_lo:[1,0] neg_hi:[1,0]
	v_pk_add_f32 v[38:39], v[202:203], v[14:15] op_sel_hi:[0,1] neg_lo:[1,0] neg_hi:[1,0]
	s_waitcnt lgkmcnt(11)
	v_pk_add_f32 v[56:57], v[202:203], v[16:17] op_sel_hi:[0,1] neg_lo:[1,0] neg_hi:[1,0]
	s_waitcnt lgkmcnt(9)
	v_pk_add_f32 v[40:41], v[202:203], v[24:25] op_sel_hi:[0,1] neg_lo:[1,0] neg_hi:[1,0]
	v_pk_add_f32 v[58:59], v[202:203], v[18:19] op_sel_hi:[0,1] neg_lo:[1,0] neg_hi:[1,0]
	v_pk_add_f32 v[42:43], v[202:203], v[26:27] op_sel_hi:[0,1] neg_lo:[1,0] neg_hi:[1,0]
	v_pk_add_f32 v[60:61], v[202:203], v[20:21] op_sel_hi:[0,1] neg_lo:[1,0] neg_hi:[1,0]
	s_waitcnt lgkmcnt(8)
	v_pk_add_f32 v[44:45], v[202:203], v[28:29] op_sel_hi:[0,1] neg_lo:[1,0] neg_hi:[1,0]
	v_pk_add_f32 v[62:63], v[202:203], v[22:23] op_sel_hi:[0,1] neg_lo:[1,0] neg_hi:[1,0]
	v_pk_add_f32 v[46:47], v[202:203], v[30:31] op_sel_hi:[0,1] neg_lo:[1,0] neg_hi:[1,0]
	s_andn2_b64 vcc, exec, s[2:3]
	v_cmp_gt_u32_e64 s[2:3], 32, v199
	v_lshl_add_u32 v219, v236, 2, s19
	v_lshlrev_b32_e32 v204, 4, v0
	s_cbranch_vccnz .LBB0_742
	s_lshl_b64 s[18:19], s[4:5], 1
	s_add_u32 s18, s70, s18
	s_addc_u32 s19, s71, s19
	s_add_u32 s18, s18, s14
	s_addc_u32 s19, s19, s15
	v_lshl_add_u64 v[206:207], s[18:19], 0, v[96:97]
	s_lshl_b64 s[18:19], s[16:17], 1
	s_add_u32 s18, s18, s14
	v_mov_b32_e32 v205, v97
	s_addc_u32 s19, s19, s15
	v_lshl_add_u64 v[0:1], s[18:19], 0, v[204:205]
	s_lshl_b32 s18, s41, 9
	s_and_b32 s18, s18, 0x18000
	v_lshl_or_b32 v2, v241, 11, s18
	v_mov_b32_e32 v3, v97
	v_lshl_add_u64 v[0:1], v[0:1], 0, v[2:3]
	v_mov_b32_e32 v16, v97
	v_mov_b32_e32 v17, v97
	v_lshl_add_u64 v[208:209], s[70:71], 0, v[0:1]
	v_subrev_u32_e32 v245, s14, v0
	v_add_u32_e32 v245, 0x7fc0000, v245
	v_lshl_add_u32 v244, s4, 1, v96
	s_add_u32 s98, s70, s14
	s_addc_u32 s99, s71, s15
	s_add_u32 s98, s98, s12
	s_addc_u32 s99, s99, s13
	s_add_u32 s98, s98, 0x16e80000
	s_addc_u32 s99, s99, 0
	v_readlane_b32 s18, v253, 11
	v_mov_b32_e32 v18, v97
	v_mov_b32_e32 v19, v97
	v_mov_b32_e32 v20, v97
	v_mov_b32_e32 v21, v97
	v_mov_b32_e32 v22, v97
	v_mov_b32_e32 v23, v97
	v_mov_b32_e32 v24, v97
	v_mov_b32_e32 v25, v97
	v_mov_b32_e32 v26, v97
	v_mov_b32_e32 v27, v97
	v_mov_b32_e32 v28, v97
	v_mov_b32_e32 v29, v97
	v_mov_b32_e32 v30, v97
	v_mov_b32_e32 v31, v97
	v_mov_b64_e32 v[0:1], v[16:17]
	v_lshl_add_u32 v205, v215, 4, s18
	s_mov_b32 s18, 0
	s_movk_i32 s22, 0x4000
	s_movk_i32 s38, 0x2000
	v_mov_b32_e32 v240, 0
	s_mov_b32 s23, 6
	v_mov_b64_e32 v[2:3], v[18:19]
	v_mov_b64_e32 v[4:5], v[20:21]
	v_mov_b64_e32 v[6:7], v[22:23]
	v_mov_b64_e32 v[8:9], v[24:25]
	v_mov_b64_e32 v[10:11], v[26:27]
	v_mov_b64_e32 v[12:13], v[28:29]
	v_mov_b64_e32 v[14:15], v[30:31]
	s_nop 0
	s_nop 0
	s_nop 0
	s_nop 0
	s_nop 0
	s_nop 0
	s_nop 0
